# post0 rope: nested EXEC diamonds flattened onto two loop-invariant lane masks (bodies unchanged), on top of the combined variant
# baseline (speedup 1.0000x reference)
.LBB0_556:
	s_or_b64 exec, exec, s[2:3]
	v_ashrrev_i32_e32 v3, 6, v3
	v_lshl_add_u32 v94, s94, 3, v3
	s_movk_i32 s2, 0x4000
	v_cmp_gt_i32_e32 vcc, s2, v94
	s_and_saveexec_b64 s[18:19], vcc
	s_cbranch_execz .LBB0_831
	v_mbcnt_lo_u32_b32 v3, -1, 0
	v_mbcnt_hi_u32_b32 v3, -1, v3
	v_and_b32_e32 v5, 64, v3
	v_xor_b32_e32 v4, 1, v3
	v_add_u32_e32 v6, 64, v5
	v_cmp_lt_i32_e32 vcc, v4, v6
	v_and_b32_e32 v96, 7, v2
	v_and_b32_e32 v8, 15, v2
	v_cndmask_b32_e32 v4, v3, v4, vcc
	v_lshlrev_b32_e32 v208, 2, v4
	v_xor_b32_e32 v4, 2, v3
	v_cmp_lt_i32_e32 vcc, v4, v6
	v_mov_b32_e32 v99, 0
	s_mov_b64 s[2:3], 0x5ed10000
	v_cndmask_b32_e32 v4, v3, v4, vcc
	v_lshlrev_b32_e32 v209, 2, v4
	v_xor_b32_e32 v4, 4, v3
	v_cmp_lt_i32_e32 vcc, v4, v6
	v_readlane_b32 s64, v254, 2
	v_mov_b32_e32 v7, v99
	v_cndmask_b32_e32 v4, v3, v4, vcc
	v_lshlrev_b32_e32 v210, 2, v4
	v_and_b32_e32 v4, 48, v2
	v_cmp_eq_u32_e64 s[4:5], 16, v4
	v_xor_b32_e32 v4, 32, v3
	v_cmp_lt_i32_e32 vcc, v4, v6
	v_lshlrev_b32_e32 v2, 1, v2
	v_and_b32_e32 v215, 48, v2
	v_cndmask_b32_e32 v4, v3, v4, vcc
	v_lshlrev_b32_e32 v211, 2, v4
	v_xor_b32_e32 v4, 16, v3
	v_cmp_lt_i32_e32 vcc, v4, v6
	v_lshlrev_b32_e32 v2, 5, v1
	v_readlane_b32 s74, v254, 12
	v_cndmask_b32_e32 v4, v3, v4, vcc
	v_lshlrev_b32_e32 v212, 2, v4
	v_xor_b32_e32 v4, 8, v3
	v_cmp_lt_i32_e32 vcc, v4, v6
	v_or_b32_e32 v6, 0x1000, v2
	v_readlane_b32 s75, v254, 13
	v_cndmask_b32_e32 v4, v3, v4, vcc
	v_lshlrev_b32_e32 v213, 2, v4
	v_or_b32_e32 v4, v5, v96
	v_lshl_or_b32 v214, v4, 2, 64
	v_and_b32_e32 v4, 0x400, v2
	v_mov_b32_e32 v5, v99
	v_lshlrev_b32_e32 v3, 2, v3
	v_lshl_add_u64 v[4:5], s[88:89], 0, v[4:5]
	v_and_b32_e32 v216, 0x100, v3
	v_mov_b32_e32 v3, v99
	v_lshl_add_u64 v[100:101], v[4:5], 0, s[2:3]
	v_lshlrev_b32_e32 v4, 6, v96
	v_mov_b32_e32 v5, v99
	v_readlane_b32 s76, v254, 14
	v_readlane_b32 s77, v254, 15
	v_lshl_add_u64 v[110:111], s[48:49], 0, v[2:3]
	s_mov_b64 s[2:3], 0x4800
	v_lshl_add_u64 v[118:119], s[48:49], 0, v[6:7]
	v_ashrrev_i32_e32 v95, 31, v94
	v_lshl_add_u64 v[102:103], s[74:75], 0, v[4:5]
	v_lshl_add_u64 v[104:105], s[76:77], 0, v[4:5]
	v_lshlrev_b32_e32 v4, 2, v1
	v_lshl_add_u64 v[112:113], v[110:111], 0, s[2:3]
	v_lshl_add_u64 v[116:117], s[50:51], 0, v[6:7]
	v_lshl_add_u64 v[120:121], v[118:119], 0, s[2:3]
	s_mov_b64 s[2:3], 0x1800
	v_lshlrev_b64 v[6:7], 5, v[94:95]
	v_lshl_add_u64 v[124:125], v[110:111], 0, s[2:3]
	v_lshl_add_u64 v[132:133], v[118:119], 0, s[2:3]
	v_lshl_add_u64 v[6:7], v[6:7], 0, v[4:5]
	s_mov_b64 s[2:3], 0x5ef10000
	v_lshl_add_u64 v[140:141], v[6:7], 0, s[2:3]
	v_lshlrev_b64 v[6:7], 6, v[94:95]
	v_lshl_add_u64 v[6:7], v[6:7], 0, v[4:5]
	s_mov_b64 s[2:3], 0x5ef90000
	v_lshlrev_b32_e32 v10, 5, v8
	v_lshl_add_u64 v[142:143], v[6:7], 0, s[2:3]
	s_movk_i32 s2, 0xc00
	v_lshlrev_b32_e32 v9, 4, v96
	v_and_b32_e32 v11, 0x100, v10
	v_lshlrev_b64 v[138:139], 9, v[94:95]
	v_mad_i64_i32 v[144:145], s[2:3], v94, s2, 0
	v_lshlrev_b64 v[6:7], 10, v[94:95]
	v_readlane_b32 s78, v254, 16
	v_readlane_b32 s79, v254, 17
	v_or3_b32 v138, v138, v11, v9
	v_lshl_or_b32 v8, v8, 2, v6
	v_mov_b32_e32 v9, v7
	s_mov_b64 s[2:3], 0x59d10120
	v_lshl_add_u64 v[106:107], s[78:79], 0, v[4:5]
	s_mov_b64 s[8:9], 0x5000
	v_lshl_add_u64 v[122:123], s[52:53], 0, v[4:5]
	v_lshl_add_u64 v[148:149], v[8:9], 0, s[2:3]
	v_or_b32_e32 v4, v6, v4
	v_mov_b32_e32 v5, v7
	s_mov_b64 s[2:3], 0x59d10000
	v_lshlrev_b32_e32 v98, 4, v1
	v_lshl_add_u64 v[114:115], v[110:111], 0, s[8:9]
	s_mov_b64 s[8:9], 0x3000
	v_lshl_add_u64 v[150:151], v[4:5], 0, s[2:3]
	v_lshl_or_b32 v4, v96, 2, v6
	s_mov_b64 s[2:3], 0x59d10100
	s_lshl_b32 s20, s92, 3
	v_lshl_add_u64 v[126:127], v[110:111], 0, s[8:9]
	s_mov_b64 s[10:11], 0x2000
	v_lshl_add_u64 v[134:135], v[118:119], 0, s[8:9]
	v_lshl_add_u64 v[152:153], v[4:5], 0, s[2:3]
	v_or_b32_e32 v6, v6, v98
	s_mov_b64 s[2:3], 0x5dd10000
	s_movk_i32 s8, 0x2600
	v_readlane_b32 s65, v254, 3
	v_readlane_b32 s66, v254, 4
	v_readlane_b32 s67, v254, 5
	v_readlane_b32 s68, v254, 6
	v_readlane_b32 s69, v254, 7
	v_readlane_b32 s70, v254, 8
	v_readlane_b32 s71, v254, 9
	v_lshl_add_u64 v[128:129], v[110:111], 0, s[10:11]
	s_mov_b64 s[10:11], 0x3800
	s_ashr_i32 s21, s20, 31
	v_lshlrev_b64 v[146:147], 11, v[94:95]
	v_lshl_add_u64 v[154:155], v[6:7], 0, s[2:3]
	v_mad_i64_i32 v[156:157], s[2:3], v94, s8, 0
	v_cmp_gt_u32_e64 s[6:7], 8, v1
	v_or_b32_e32 v217, 4, v216
	v_or_b32_e32 v218, 8, v216
	v_or_b32_e32 v219, 12, v216
	v_or_b32_e32 v220, 16, v216
	v_or_b32_e32 v221, 20, v216
	v_or_b32_e32 v222, 24, v216
	v_or_b32_e32 v223, 28, v216
	v_or_b32_e32 v224, 32, v216
	v_or_b32_e32 v225, 36, v216
	v_or_b32_e32 v226, 40, v216
	v_or_b32_e32 v227, 44, v216
	v_or_b32_e32 v228, 48, v216
	v_or_b32_e32 v229, 52, v216
	v_or_b32_e32 v230, 56, v216
	v_or_b32_e32 v231, 60, v216
	v_or_b32_e32 v232, 64, v216
	v_or_b32_e32 v233, 0x44, v216
	v_or_b32_e32 v234, 0x48, v216
	v_or_b32_e32 v235, 0x4c, v216
	v_or_b32_e32 v236, 0x50, v216
	v_or_b32_e32 v237, 0x54, v216
	v_or_b32_e32 v238, 0x58, v216
	v_or_b32_e32 v239, 0x5c, v216
	v_lshl_add_u64 v[108:109], s[50:51], 0, v[2:3]
	v_lshl_add_u64 v[130:131], v[110:111], 0, s[10:11]
	v_lshl_add_u64 v[136:137], v[94:95], 2, s[66:67]
	s_lshl_b64 s[22:23], s[20:21], 2
	s_lshl_b64 s[24:25], s[20:21], 9
	s_lshl_b64 s[26:27], s[20:21], 5
	s_lshl_b64 s[28:29], s[20:21], 6
	v_or_b32_e32 v144, v144, v98
	s_mul_i32 s30, s92, 0x6000
	s_mul_hi_i32 s31, s20, 0xc00
	v_or_b32_e32 v146, v146, v2
	s_lshl_b64 s[34:35], s[20:21], 11
	s_lshl_b64 s[36:37], s[20:21], 10
	v_mad_i64_i32 v[158:159], s[2:3], v94, s8, v[98:99]
	s_mul_i32 s38, s92, 0x13000
	s_mul_hi_i32 s39, s20, 0x2600
	v_or_b32_e32 v156, v156, v10
	v_mad_i64_i32 v[160:161], s[2:3], v94, s8, v[2:3]
	s_mov_b64 s[40:41], 0
	s_mov_b64 s[42:43], 0x39d10000
	s_mov_b32 s21, 0x39d10000
	s_mov_b64 s[44:45], 0x39d10800
	s_mov_b64 s[46:47], 0x39d10a00
	s_mov_b32 s33, 0x39d11000
	s_mov_b32 s48, 0x39d12000
	s_brev_b32 s49, 18
	s_mov_b32 s50, 0x800000
	s_mov_b32 s51, 0xfe5163ab
	s_mov_b32 s52, 0x3c439041
	s_mov_b32 s53, 0xdb629599
	s_mov_b32 s60, 0xf534ddc0
	s_mov_b32 s61, 0xfc2757d1
	s_mov_b32 s62, 0x4e441529
	s_mov_b32 s63, 0xa2f9836e
	s_mov_b32 s64, 0x3fc90fda
	s_mov_b32 s65, 0x3f22f983
	s_mov_b32 s66, 0xbfc90fda
	s_brev_b32 s67, 1
	s_movk_i32 s68, 0x1f8
	v_mov_b32_e32 v95, 0x358637bd
	s_mov_b32 s69, 0x5ad10000
	v_lshlrev_b32_e32 v162, 1, v96
	s_mov_b32 s70, 0x41a00000
	s_mov_b32 s71, 0x3fb8aa3b
	s_mov_b32 s74, 0xc2ce8ed0
	s_mov_b32 s75, 0x42b17218
	s_mov_b32 s76, 0x7f800000
	s_mov_b32 s77, 0x3f2aaaab
	s_mov_b32 s78, 0x3f317218
	s_mov_b32 s79, 0x33800000
	s_mov_b32 s80, 0x5f090000
	v_mov_b32_e32 v243, 0xffff8e00
	v_mov_b32_e32 v246, 0xffffb400
	v_mov_b32_e32 v242, 0xffffda00
	v_not_b32_e32 v244, 31
	v_mov_b32_e32 v245, 0x7fc00000
	v_mov_b32_e32 v164, 0x3f317218
	s_movk_i32 s81, 0x3fff
	v_readlane_b32 s72, v254, 10
	v_readlane_b32 s73, v254, 11
	v_cmp_eq_u32_e64 s[82:83], 1, v96
	v_cmp_eq_u32_e64 s[84:85], 0, v96
	s_branch .LBB0_559

.LBB0_561:
	s_andn2_saveexec_b64 s[2:3], s[2:3]
	v_mul_f32_e64 v71, |v1|, s65
	v_rndne_f32_e32 v73, v71
	v_cvt_i32_f32_e32 v72, v73
	v_fma_f32 v71, v73, s66, |v1|
	v_fmac_f32_e32 v71, 0xb3a22168, v73
	v_fmac_f32_e32 v71, 0xa7c234c4, v73
	s_or_b64 exec, exec, s[2:3]
	v_mul_f32_e32 v73, v71, v71
	v_mov_b32_e32 v74, 0x3c0881c4
	v_fmamk_f32 v74, v73, 0xb94c1982, v74
	v_fmaak_f32 v74, v73, v74, 0xbe2aaa9d
	v_mul_f32_e32 v74, v73, v74
	v_fmac_f32_e32 v71, v71, v74
	v_mov_b32_e32 v74, 0xbab64f3b
	v_fmamk_f32 v74, v73, 0x37d75334, v74
	v_fmaak_f32 v74, v73, v74, 0x3d2aabf7
	v_fmaak_f32 v74, v73, v74, 0xbf000004
	global_load_dwordx4 v[78:81], v[102:103], off offset:16
	global_load_dwordx4 v[90:93], v[102:103], off
	v_fma_f32 v73, v73, v74, 1.0
	v_lshlrev_b32_e32 v74, 30, v72
	v_and_b32_e32 v72, 1, v72
	v_cmp_eq_u32_e32 vcc, 0, v72
	v_xor_b32_e32 v70, v70, v1
	v_and_b32_e32 v75, 0x80000000, v74
	v_cndmask_b32_e32 v72, v73, v71, vcc
	v_xor_b32_e32 v71, 0x80000000, v71
	v_xor_b32_e32 v70, v70, v72
	v_cndmask_b32_e32 v71, v71, v73, vcc
	v_xor_b32_e32 v70, v70, v75
	v_bitop3_b32 v71, v71, v74, s67 bitop3:0x78
	v_cmp_class_f32_e64 vcc, v1, s68
	v_lshlrev_b32_e32 v250, 16, v82
	v_and_b32_e32 v251, 0xffff0000, v82
	v_cndmask_b32_e32 v98, v245, v71, vcc
	v_cndmask_b32_e32 v163, v245, v70, vcc
	global_load_dwordx4 v[70:73], v[102:103], off offset:48
	global_load_dwordx4 v[74:77], v[102:103], off offset:32
	v_lshlrev_b32_e32 v206, 16, v83
	v_and_b32_e32 v207, 0xffff0000, v83
	v_pk_mul_f32 v[82:83], v[250:251], v[250:251]
	v_pk_mul_f32 v[172:173], v[206:207], v[206:207]
	v_add_f32_e32 v1, v82, v83
	v_lshlrev_b32_e32 v204, 16, v84
	v_and_b32_e32 v205, 0xffff0000, v84
	v_add_f32_e32 v1, v172, v1
	v_lshlrev_b32_e32 v202, 16, v85
	v_and_b32_e32 v203, 0xffff0000, v85
	v_pk_mul_f32 v[84:85], v[204:205], v[204:205]
	v_add_f32_e32 v1, v173, v1
	v_add_f32_e32 v1, v84, v1
	v_pk_mul_f32 v[170:171], v[202:203], v[202:203]
	v_add_f32_e32 v1, v85, v1
	v_lshlrev_b32_e32 v200, 16, v86
	v_and_b32_e32 v201, 0xffff0000, v86
	v_add_f32_e32 v1, v170, v1
	v_lshlrev_b32_e32 v198, 16, v87
	v_and_b32_e32 v199, 0xffff0000, v87
	v_pk_mul_f32 v[86:87], v[200:201], v[200:201]
	v_add_f32_e32 v1, v171, v1
	v_add_f32_e32 v1, v86, v1
	v_pk_mul_f32 v[168:169], v[198:199], v[198:199]
	v_add_f32_e32 v1, v87, v1
	v_lshlrev_b32_e32 v196, 16, v88
	v_and_b32_e32 v197, 0xffff0000, v88
	v_add_f32_e32 v1, v168, v1
	v_lshlrev_b32_e32 v194, 16, v89
	v_and_b32_e32 v195, 0xffff0000, v89
	v_pk_mul_f32 v[88:89], v[196:197], v[196:197]
	v_add_f32_e32 v1, v169, v1
	v_add_f32_e32 v1, v88, v1
	v_pk_mul_f32 v[166:167], v[194:195], v[194:195]
	v_add_f32_e32 v1, v89, v1
	v_add_f32_e32 v1, v166, v1
	v_add_f32_e32 v1, v167, v1
	s_nop 1
	v_mov_b32_dpp v82, v1 quad_perm:[1,0,3,2] row_mask:0xf bank_mask:0xf
	ds_bpermute_b32 v192, v216, v98
	ds_bpermute_b32 v193, v216, v163
	ds_bpermute_b32 v190, v217, v98
	ds_bpermute_b32 v191, v217, v163
	s_waitcnt lgkmcnt(4)
	v_add_f32_e32 v1, v1, v82
	ds_bpermute_b32 v82, v209, v1
	ds_bpermute_b32 v188, v218, v98
	ds_bpermute_b32 v189, v218, v163
	ds_bpermute_b32 v186, v219, v98
	ds_bpermute_b32 v187, v219, v163
	s_waitcnt lgkmcnt(4)
	v_add_f32_e32 v1, v1, v82
	ds_bpermute_b32 v82, v210, v1
	ds_bpermute_b32 v184, v220, v98
	ds_bpermute_b32 v185, v220, v163
	ds_bpermute_b32 v182, v221, v98
	ds_bpermute_b32 v183, v221, v163
	s_waitcnt lgkmcnt(4)
	v_add_f32_e32 v1, v1, v82
	v_fmamk_f32 v1, v1, 0x3c000000, v95
	v_mul_f32_e32 v82, 0x4b800000, v1
	v_cmp_gt_f32_e32 vcc, s50, v1
	ds_bpermute_b32 v180, v222, v98
	ds_bpermute_b32 v181, v222, v163
	v_cndmask_b32_e32 v1, v1, v82, vcc
	v_rsq_f32_e32 v1, v1
	ds_bpermute_b32 v178, v223, v98
	ds_bpermute_b32 v179, v223, v163
	ds_bpermute_b32 v176, v224, v98
	v_mul_f32_e32 v82, 0x45800000, v1
	v_cndmask_b32_e32 v84, v1, v82, vcc
	v_mov_b32_e32 v85, v84
	v_pk_mul_f32 v[82:83], v[84:85], v[250:251] op_sel_hi:[0,1]
	s_waitcnt vmcnt(2)
	v_pk_mul_f32 v[82:83], v[90:91], v[82:83]
	ds_bpermute_b32 v177, v224, v163
	ds_bpermute_b32 v174, v225, v98
	ds_bpermute_b32 v175, v225, v163
	ds_bpermute_b32 v172, v226, v98
	ds_bpermute_b32 v173, v226, v163
	ds_bpermute_b32 v170, v227, v98
	ds_bpermute_b32 v171, v227, v163
	ds_bpermute_b32 v168, v228, v98
	ds_bpermute_b32 v169, v228, v163
	ds_bpermute_b32 v166, v229, v98
	ds_bpermute_b32 v167, v229, v163
	ds_bpermute_b32 v88, v230, v98
	ds_bpermute_b32 v89, v230, v163
	ds_bpermute_b32 v86, v231, v98
	ds_bpermute_b32 v87, v231, v163
	s_nop 1
	v_mov_b32_dpp v91, v82 quad_perm:[1,0,3,2] row_mask:0xf bank_mask:0xf
	s_mov_b64 s[2:3], exec
	s_and_b64 exec, s[2:3], s[82:83]
	v_mov_b32_e32 v90, v82
	s_waitcnt lgkmcnt(0)
	v_pk_mul_f32 v[90:91], v[90:91], v[192:193]
	s_nop 0
	v_add_f32_e32 v82, v90, v91
	s_and_b64 exec, s[2:3], s[84:85]
	v_mov_b32_e32 v90, v82
	s_waitcnt lgkmcnt(0)
	v_pk_mul_f32 v[90:91], v[90:91], v[192:193]
	s_nop 0
	v_sub_f32_e32 v82, v90, v91
	s_mov_b64 exec, s[2:3]
	s_waitcnt lgkmcnt(0)
	s_nop 1
	v_mov_b32_dpp v91, v83 quad_perm:[1,0,3,2] row_mask:0xf bank_mask:0xf
	s_mov_b64 s[2:3], exec
	s_and_b64 exec, s[2:3], s[82:83]
	v_mov_b32_e32 v250, v83
	v_mov_b32_e32 v251, v191
	v_mov_b32_e32 v90, v190
	v_mul_f32_e32 v252, v83, v190
	s_waitcnt lgkmcnt(0)
	v_pk_fma_f32 v[90:91], v[250:251], v[90:91], v[252:253] op_sel_hi:[1,1,0]
	s_nop 0
	v_mov_b32_e32 v83, v91
	s_and_b64 exec, s[2:3], s[84:85]
	v_mov_b32_e32 v250, v83
	v_mov_b32_e32 v251, v191
	v_mov_b32_e32 v90, v190
	v_mul_f32_e32 v252, v83, v190
	s_waitcnt lgkmcnt(0)
	v_pk_fma_f32 v[90:91], v[250:251], v[90:91], v[252:253] op_sel_hi:[1,1,0] neg_lo:[1,0,0] neg_hi:[1,0,0]
	s_nop 0
	v_mov_b32_e32 v83, v91
	s_mov_b64 exec, s[2:3]
	s_waitcnt lgkmcnt(0)
	v_pk_mul_f32 v[90:91], v[84:85], v[206:207]
	v_pk_mul_f32 v[90:91], v[92:93], v[90:91]
	s_nop 1
	v_mov_b32_dpp v93, v90 quad_perm:[1,0,3,2] row_mask:0xf bank_mask:0xf
	s_mov_b64 s[2:3], exec
	s_and_b64 exec, s[2:3], s[82:83]
	v_mov_b32_e32 v92, v90
	s_waitcnt lgkmcnt(0)
	v_pk_mul_f32 v[92:93], v[92:93], v[188:189]
	s_nop 0
	v_add_f32_e32 v90, v92, v93
	s_and_b64 exec, s[2:3], s[84:85]
	v_mov_b32_e32 v92, v90
	s_waitcnt lgkmcnt(0)
	v_pk_mul_f32 v[92:93], v[92:93], v[188:189]
	s_nop 0
	v_sub_f32_e32 v90, v92, v93
	s_mov_b64 exec, s[2:3]
	s_waitcnt lgkmcnt(0)
	s_nop 1
	v_mov_b32_dpp v93, v91 quad_perm:[1,0,3,2] row_mask:0xf bank_mask:0xf
	s_mov_b64 s[2:3], exec
	s_and_b64 exec, s[2:3], s[82:83]
	v_mov_b32_e32 v206, v91
	v_mov_b32_e32 v207, v187
	v_mov_b32_e32 v92, v186
	v_mul_f32_e32 v250, v91, v186
	s_waitcnt lgkmcnt(0)
	v_pk_fma_f32 v[92:93], v[206:207], v[92:93], v[250:251] op_sel_hi:[1,1,0]
	s_nop 0
	v_mov_b32_e32 v91, v93
	s_and_b64 exec, s[2:3], s[84:85]
	v_mov_b32_e32 v206, v91
	v_mov_b32_e32 v207, v187
	v_mov_b32_e32 v92, v186
	v_mul_f32_e32 v250, v91, v186
	s_waitcnt lgkmcnt(0)
	v_pk_fma_f32 v[92:93], v[206:207], v[92:93], v[250:251] op_sel_hi:[1,1,0] neg_lo:[1,0,0] neg_hi:[1,0,0]
	s_nop 0
	v_mov_b32_e32 v91, v93
	s_mov_b64 exec, s[2:3]
	s_waitcnt lgkmcnt(0)
	v_pk_mul_f32 v[92:93], v[84:85], v[204:205]
	v_pk_mul_f32 v[78:79], v[78:79], v[92:93]
	s_nop 1
	v_mov_b32_dpp v93, v78 quad_perm:[1,0,3,2] row_mask:0xf bank_mask:0xf
	s_mov_b64 s[2:3], exec
	s_and_b64 exec, s[2:3], s[82:83]
	v_mov_b32_e32 v92, v78
	s_waitcnt lgkmcnt(0)
	v_pk_mul_f32 v[92:93], v[92:93], v[184:185]
	s_nop 0
	v_add_f32_e32 v78, v92, v93
	s_and_b64 exec, s[2:3], s[84:85]
	v_mov_b32_e32 v92, v78
	s_waitcnt lgkmcnt(0)
	v_pk_mul_f32 v[92:93], v[92:93], v[184:185]
	s_nop 0
	v_sub_f32_e32 v78, v92, v93
	s_mov_b64 exec, s[2:3]
	s_waitcnt lgkmcnt(0)
	s_nop 1
	v_mov_b32_dpp v93, v79 quad_perm:[1,0,3,2] row_mask:0xf bank_mask:0xf
	s_mov_b64 s[2:3], exec
	s_and_b64 exec, s[2:3], s[82:83]
	v_mov_b32_e32 v204, v79
	v_mov_b32_e32 v205, v183
	v_mov_b32_e32 v92, v182
	v_mul_f32_e32 v206, v79, v182
	s_waitcnt lgkmcnt(0)
	v_pk_fma_f32 v[92:93], v[204:205], v[92:93], v[206:207] op_sel_hi:[1,1,0]
	s_nop 0
	v_mov_b32_e32 v79, v93
	s_and_b64 exec, s[2:3], s[84:85]
	v_mov_b32_e32 v204, v79
	v_mov_b32_e32 v205, v183
	v_mov_b32_e32 v92, v182
	v_mul_f32_e32 v206, v79, v182
	s_waitcnt lgkmcnt(0)
	v_pk_fma_f32 v[92:93], v[204:205], v[92:93], v[206:207] op_sel_hi:[1,1,0] neg_lo:[1,0,0] neg_hi:[1,0,0]
	s_nop 0
	v_mov_b32_e32 v79, v93
	s_mov_b64 exec, s[2:3]
	s_waitcnt lgkmcnt(0)
	v_pk_mul_f32 v[92:93], v[84:85], v[202:203]
	v_pk_mul_f32 v[80:81], v[80:81], v[92:93]
	s_nop 1
	v_mov_b32_dpp v93, v80 quad_perm:[1,0,3,2] row_mask:0xf bank_mask:0xf
	s_mov_b64 s[2:3], exec
	s_and_b64 exec, s[2:3], s[82:83]
	v_mov_b32_e32 v92, v80
	s_waitcnt lgkmcnt(0)
	v_pk_mul_f32 v[92:93], v[92:93], v[180:181]
	s_nop 0
	v_add_f32_e32 v80, v92, v93
	s_and_b64 exec, s[2:3], s[84:85]
	v_mov_b32_e32 v92, v80
	s_waitcnt lgkmcnt(0)
	v_pk_mul_f32 v[92:93], v[92:93], v[180:181]
	s_nop 0
	v_sub_f32_e32 v80, v92, v93
	s_mov_b64 exec, s[2:3]
	s_waitcnt lgkmcnt(0)
	s_nop 1
	v_mov_b32_dpp v93, v81 quad_perm:[1,0,3,2] row_mask:0xf bank_mask:0xf
	s_mov_b64 s[2:3], exec
	s_and_b64 exec, s[2:3], s[82:83]
	v_mov_b32_e32 v202, v81
	v_mov_b32_e32 v203, v179
	v_mov_b32_e32 v92, v178
	v_mul_f32_e32 v204, v81, v178
	s_waitcnt lgkmcnt(0)
	v_pk_fma_f32 v[92:93], v[202:203], v[92:93], v[204:205] op_sel_hi:[1,1,0]
	s_nop 0
	v_mov_b32_e32 v81, v93
	s_and_b64 exec, s[2:3], s[84:85]
	v_mov_b32_e32 v202, v81
	v_mov_b32_e32 v203, v179
	v_mov_b32_e32 v92, v178
	v_mul_f32_e32 v204, v81, v178
	s_waitcnt lgkmcnt(0)
	v_pk_fma_f32 v[92:93], v[202:203], v[92:93], v[204:205] op_sel_hi:[1,1,0] neg_lo:[1,0,0] neg_hi:[1,0,0]
	s_nop 0
	v_mov_b32_e32 v81, v93
	s_mov_b64 exec, s[2:3]
	s_waitcnt lgkmcnt(0)
	v_pk_mul_f32 v[92:93], v[84:85], v[200:201]
	s_waitcnt vmcnt(0)
	v_pk_mul_f32 v[74:75], v[74:75], v[92:93]
	s_nop 1
	v_mov_b32_dpp v93, v74 quad_perm:[1,0,3,2] row_mask:0xf bank_mask:0xf
	s_mov_b64 s[2:3], exec
	s_and_b64 exec, s[2:3], s[82:83]
	v_mov_b32_e32 v92, v74
	s_waitcnt lgkmcnt(0)
	v_pk_mul_f32 v[92:93], v[92:93], v[176:177]
	s_nop 0
	v_add_f32_e32 v74, v92, v93
	s_and_b64 exec, s[2:3], s[84:85]
	v_mov_b32_e32 v92, v74
	s_waitcnt lgkmcnt(0)
	v_pk_mul_f32 v[92:93], v[92:93], v[176:177]
	s_nop 0
	v_sub_f32_e32 v74, v92, v93
	s_mov_b64 exec, s[2:3]
	s_waitcnt lgkmcnt(0)
	s_nop 1
	v_mov_b32_dpp v93, v75 quad_perm:[1,0,3,2] row_mask:0xf bank_mask:0xf
	s_mov_b64 s[2:3], exec
	s_and_b64 exec, s[2:3], s[82:83]
	v_mov_b32_e32 v200, v75
	v_mov_b32_e32 v201, v175
	v_mov_b32_e32 v92, v174
	v_mul_f32_e32 v202, v75, v174
	s_waitcnt lgkmcnt(0)
	v_pk_fma_f32 v[92:93], v[200:201], v[92:93], v[202:203] op_sel_hi:[1,1,0]
	s_nop 0
	v_mov_b32_e32 v75, v93
	s_and_b64 exec, s[2:3], s[84:85]
	v_mov_b32_e32 v200, v75
	v_mov_b32_e32 v201, v175
	v_mov_b32_e32 v92, v174
	v_mul_f32_e32 v202, v75, v174
	s_waitcnt lgkmcnt(0)
	v_pk_fma_f32 v[92:93], v[200:201], v[92:93], v[202:203] op_sel_hi:[1,1,0] neg_lo:[1,0,0] neg_hi:[1,0,0]
	s_nop 0
	v_mov_b32_e32 v75, v93
	s_mov_b64 exec, s[2:3]
	s_waitcnt lgkmcnt(0)
	v_pk_mul_f32 v[92:93], v[84:85], v[198:199]
	v_pk_mul_f32 v[76:77], v[92:93], v[76:77]
	s_nop 1
	v_mov_b32_dpp v93, v76 quad_perm:[1,0,3,2] row_mask:0xf bank_mask:0xf
	s_mov_b64 s[2:3], exec
	s_and_b64 exec, s[2:3], s[82:83]
	v_mov_b32_e32 v92, v76
	s_waitcnt lgkmcnt(0)
	v_pk_mul_f32 v[92:93], v[92:93], v[172:173]
	s_nop 0
	v_add_f32_e32 v76, v92, v93
	s_and_b64 exec, s[2:3], s[84:85]
	v_mov_b32_e32 v92, v76
	s_waitcnt lgkmcnt(0)
	v_pk_mul_f32 v[92:93], v[92:93], v[172:173]
	s_nop 0
	v_sub_f32_e32 v76, v92, v93
	s_mov_b64 exec, s[2:3]
	s_waitcnt lgkmcnt(0)
	s_nop 1
	v_mov_b32_dpp v93, v77 quad_perm:[1,0,3,2] row_mask:0xf bank_mask:0xf
	s_mov_b64 s[2:3], exec
	s_and_b64 exec, s[2:3], s[82:83]
	v_mov_b32_e32 v198, v77
	v_mov_b32_e32 v199, v171
	v_mov_b32_e32 v92, v170
	v_mul_f32_e32 v200, v77, v170
	s_waitcnt lgkmcnt(0)
	v_pk_fma_f32 v[92:93], v[198:199], v[92:93], v[200:201] op_sel_hi:[1,1,0]
	s_nop 0
	v_mov_b32_e32 v77, v93
	s_and_b64 exec, s[2:3], s[84:85]
	v_mov_b32_e32 v198, v77
	v_mov_b32_e32 v199, v171
	v_mov_b32_e32 v92, v170
	v_mul_f32_e32 v200, v77, v170
	s_waitcnt lgkmcnt(0)
	v_pk_fma_f32 v[92:93], v[198:199], v[92:93], v[200:201] op_sel_hi:[1,1,0] neg_lo:[1,0,0] neg_hi:[1,0,0]
	s_nop 0
	v_mov_b32_e32 v77, v93
	s_mov_b64 exec, s[2:3]
	s_waitcnt lgkmcnt(0)
	v_pk_mul_f32 v[92:93], v[84:85], v[196:197]
	v_pk_mul_f32 v[70:71], v[92:93], v[70:71]
	s_nop 1
	v_mov_b32_dpp v93, v70 quad_perm:[1,0,3,2] row_mask:0xf bank_mask:0xf
	s_mov_b64 s[2:3], exec
	s_and_b64 exec, s[2:3], s[82:83]
	v_mov_b32_e32 v92, v70
	s_waitcnt lgkmcnt(0)
	v_pk_mul_f32 v[92:93], v[92:93], v[168:169]
	s_nop 0
	v_add_f32_e32 v70, v92, v93
	s_and_b64 exec, s[2:3], s[84:85]
	v_mov_b32_e32 v92, v70
	s_waitcnt lgkmcnt(0)
	v_pk_mul_f32 v[92:93], v[92:93], v[168:169]
	s_nop 0
	v_sub_f32_e32 v70, v92, v93
	s_mov_b64 exec, s[2:3]
	s_waitcnt lgkmcnt(0)
	s_nop 1
	v_mov_b32_dpp v93, v71 quad_perm:[1,0,3,2] row_mask:0xf bank_mask:0xf
	s_mov_b64 s[2:3], exec
	s_and_b64 exec, s[2:3], s[82:83]
	v_mov_b32_e32 v196, v71
	v_mov_b32_e32 v197, v167
	v_mov_b32_e32 v92, v166
	v_mul_f32_e32 v198, v71, v166
	s_waitcnt lgkmcnt(0)
	v_pk_fma_f32 v[92:93], v[196:197], v[92:93], v[198:199] op_sel_hi:[1,1,0]
	s_nop 0
	v_mov_b32_e32 v71, v93
	s_and_b64 exec, s[2:3], s[84:85]
	v_mov_b32_e32 v196, v71
	v_mov_b32_e32 v197, v167
	v_mov_b32_e32 v92, v166
	v_mul_f32_e32 v198, v71, v166
	s_waitcnt lgkmcnt(0)
	v_pk_fma_f32 v[92:93], v[196:197], v[92:93], v[198:199] op_sel_hi:[1,1,0] neg_lo:[1,0,0] neg_hi:[1,0,0]
	s_nop 0
	v_mov_b32_e32 v71, v93
	s_mov_b64 exec, s[2:3]
	v_pk_mul_f32 v[84:85], v[84:85], v[194:195]
	v_pk_mul_f32 v[72:73], v[84:85], v[72:73]
	s_nop 1
	v_mov_b32_dpp v85, v72 quad_perm:[1,0,3,2] row_mask:0xf bank_mask:0xf
	s_mov_b64 s[2:3], exec
	s_and_b64 exec, s[2:3], s[82:83]
	v_mov_b32_e32 v84, v72
	s_waitcnt lgkmcnt(0)
	v_pk_mul_f32 v[84:85], v[84:85], v[88:89]
	s_nop 0
	v_add_f32_e32 v72, v84, v85
	s_and_b64 exec, s[2:3], s[84:85]
	v_mov_b32_e32 v84, v72
	s_waitcnt lgkmcnt(0)
	v_pk_mul_f32 v[84:85], v[84:85], v[88:89]
	s_nop 0
	v_sub_f32_e32 v72, v84, v85
	s_mov_b64 exec, s[2:3]
	s_waitcnt lgkmcnt(0)
	s_nop 1
	v_mov_b32_dpp v85, v73 quad_perm:[1,0,3,2] row_mask:0xf bank_mask:0xf
	s_mov_b64 s[2:3], exec
	s_and_b64 exec, s[2:3], s[82:83]
	v_mov_b32_e32 v92, v73
	v_mov_b32_e32 v93, v87
	v_mov_b32_e32 v84, v86
	v_mul_f32_e32 v194, v73, v86
	s_waitcnt lgkmcnt(0)
	v_pk_fma_f32 v[84:85], v[92:93], v[84:85], v[194:195] op_sel_hi:[1,1,0]
	s_nop 0
	v_mov_b32_e32 v73, v85
	s_and_b64 exec, s[2:3], s[84:85]
	v_mov_b32_e32 v92, v73
	v_mov_b32_e32 v93, v87
	v_mov_b32_e32 v84, v86
	v_mul_f32_e32 v194, v73, v86
	s_waitcnt lgkmcnt(0)
	v_pk_fma_f32 v[84:85], v[92:93], v[84:85], v[194:195] op_sel_hi:[1,1,0] neg_lo:[1,0,0] neg_hi:[1,0,0]
	s_nop 0
	v_mov_b32_e32 v73, v85
	s_mov_b64 exec, s[2:3]
	v_lshl_add_u64 v[92:93], s[88:89], 0, v[146:147]
	v_cvt_pk_bf16_f32 v74, v74, v75
	v_cvt_pk_bf16_f32 v75, v76, v77
	v_cvt_pk_bf16_f32 v76, v70, v71
	v_add_co_u32_e32 v70, vcc, s69, v92
	v_cvt_pk_bf16_f32 v82, v82, v83
	v_cvt_pk_bf16_f32 v83, v90, v91
	v_cvt_pk_bf16_f32 v84, v78, v79
	s_waitcnt lgkmcnt(0)
	v_cvt_pk_bf16_f32 v85, v80, v81
	v_addc_co_u32_e32 v71, vcc, 0, v93, vcc
	v_cvt_pk_bf16_f32 v77, v72, v73
	global_store_dwordx4 v[70:71], v[82:85], off
	global_store_dwordx4 v[70:71], v[74:77], off offset:16
	global_load_dwordx4 v[82:85], v[104:105], off
	s_nop 0
	global_load_dwordx4 v[78:81], v[104:105], off offset:16
	global_load_dwordx4 v[70:73], v[104:105], off offset:48
	global_load_dwordx4 v[74:77], v[104:105], off offset:32
	v_lshlrev_b32_e32 v90, 16, v66
	v_and_b32_e32 v91, 0xffff0000, v66
	v_pk_mul_f32 v[92:93], v[90:91], v[90:91]
	v_lshlrev_b32_e32 v66, 16, v67
	v_and_b32_e32 v67, 0xffff0000, v67
	v_pk_mul_f32 v[202:203], v[66:67], v[66:67]
	v_add_f32_e32 v1, v92, v93
	v_lshlrev_b32_e32 v194, 16, v68
	v_and_b32_e32 v195, 0xffff0000, v68
	v_add_f32_e32 v1, v202, v1
	v_pk_mul_f32 v[204:205], v[194:195], v[194:195]
	v_add_f32_e32 v1, v203, v1
	v_lshlrev_b32_e32 v68, 16, v69
	v_and_b32_e32 v69, 0xffff0000, v69
	v_add_f32_e32 v1, v204, v1
	v_pk_mul_f32 v[206:207], v[68:69], v[68:69]
	v_add_f32_e32 v1, v205, v1
	v_lshlrev_b32_e32 v196, 16, v62
	v_and_b32_e32 v197, 0xffff0000, v62
	v_add_f32_e32 v1, v206, v1
	v_pk_mul_f32 v[250:251], v[196:197], v[196:197]
	v_add_f32_e32 v1, v207, v1
	v_lshlrev_b32_e32 v62, 16, v63
	v_and_b32_e32 v63, 0xffff0000, v63
	v_add_f32_e32 v1, v250, v1
	v_pk_mul_f32 v[252:253], v[62:63], v[62:63]
	v_add_f32_e32 v1, v251, v1
	v_lshlrev_b32_e32 v198, 16, v64
	v_and_b32_e32 v199, 0xffff0000, v64
	v_add_f32_e32 v1, v252, v1
	v_pk_mul_f32 v[240:241], v[198:199], v[198:199]
	v_add_f32_e32 v1, v253, v1
	v_lshlrev_b32_e32 v200, 16, v65
	v_and_b32_e32 v201, 0xffff0000, v65
	v_add_f32_e32 v1, v240, v1
	v_pk_mul_f32 v[64:65], v[200:201], v[200:201]
	v_add_f32_e32 v1, v241, v1
	v_add_f32_e32 v1, v64, v1
	v_add_f32_e32 v1, v65, v1
	s_nop 1
	v_mov_b32_dpp v64, v1 quad_perm:[1,0,3,2] row_mask:0xf bank_mask:0xf
	s_waitcnt lgkmcnt(0)
	v_add_f32_e32 v1, v1, v64
	ds_bpermute_b32 v64, v209, v1
	s_waitcnt lgkmcnt(0)
	v_add_f32_e32 v1, v1, v64
	ds_bpermute_b32 v64, v210, v1
	s_waitcnt lgkmcnt(0)
	v_add_f32_e32 v1, v1, v64
	v_fmamk_f32 v1, v1, 0x3c000000, v95
	v_mul_f32_e32 v64, 0x4b800000, v1
	v_cmp_gt_f32_e32 vcc, s50, v1
	s_nop 1
	v_cndmask_b32_e32 v1, v1, v64, vcc
	v_rsq_f32_e32 v1, v1
	s_nop 0
	v_mul_f32_e32 v64, 0x45800000, v1
	v_cndmask_b32_e32 v202, v1, v64, vcc
	v_mov_b32_e32 v203, v202
	v_pk_mul_f32 v[64:65], v[202:203], v[90:91] op_sel_hi:[0,1]
	v_pk_mul_f32 v[62:63], v[202:203], v[62:63]
	s_waitcnt vmcnt(3)
	v_pk_mul_f32 v[82:83], v[82:83], v[64:65]
	v_pk_mul_f32 v[64:65], v[202:203], v[66:67]
	s_nop 1
	v_mov_b32_dpp v93, v82 quad_perm:[1,0,3,2] row_mask:0xf bank_mask:0xf
	v_pk_mul_f32 v[90:91], v[84:85], v[64:65]
	v_pk_mul_f32 v[64:65], v[202:203], v[194:195]
	s_waitcnt vmcnt(0)
	v_pk_mul_f32 v[66:67], v[62:63], v[76:77]
	v_pk_mul_f32 v[84:85], v[78:79], v[64:65]
	v_pk_mul_f32 v[64:65], v[202:203], v[68:69]
	v_pk_mul_f32 v[62:63], v[202:203], v[198:199]
	v_pk_mul_f32 v[78:79], v[80:81], v[64:65]
	v_pk_mul_f32 v[64:65], v[202:203], v[196:197]
	s_nop 0
	v_pk_mul_f32 v[68:69], v[74:75], v[64:65]
	v_pk_mul_f32 v[64:65], v[62:63], v[70:71]
	v_pk_mul_f32 v[62:63], v[202:203], v[200:201]
	s_nop 0
	v_pk_mul_f32 v[62:63], v[62:63], v[72:73]
	s_mov_b64 s[2:3], exec
	s_and_b64 exec, s[2:3], s[82:83]
	v_mov_b32_e32 v92, v82
	s_waitcnt lgkmcnt(0)
	v_pk_mul_f32 v[70:71], v[92:93], v[192:193]
	s_nop 0
	v_add_f32_e32 v82, v70, v71
	s_and_b64 exec, s[2:3], s[84:85]
	v_mov_b32_e32 v92, v82
	s_waitcnt lgkmcnt(0)
	v_pk_mul_f32 v[70:71], v[92:93], v[192:193]
	s_nop 0
	v_sub_f32_e32 v82, v70, v71
	s_mov_b64 exec, s[2:3]
	s_nop 1
	v_mov_b32_dpp v71, v83 quad_perm:[1,0,3,2] row_mask:0xf bank_mask:0xf
	s_mov_b64 s[2:3], exec
	s_and_b64 exec, s[2:3], s[82:83]
	v_mov_b32_e32 v70, v83
	v_mul_f32_e32 v72, v83, v190
	s_waitcnt lgkmcnt(0)
	v_pk_fma_f32 v[70:71], v[70:71], v[190:191], v[72:73] op_sel_hi:[1,1,0]
	s_nop 0
	v_mov_b32_e32 v83, v71
	s_and_b64 exec, s[2:3], s[84:85]
	v_mov_b32_e32 v72, v83
	v_mov_b32_e32 v73, v191
	s_waitcnt lgkmcnt(0)
	v_mov_b32_e32 v191, v71
	v_mul_f32_e32 v70, v83, v190
	v_pk_fma_f32 v[70:71], v[72:73], v[190:191], v[70:71] op_sel_hi:[1,1,0] neg_lo:[1,0,0] neg_hi:[1,0,0]
	s_nop 0
	v_mov_b32_e32 v83, v71
	s_mov_b64 exec, s[2:3]
	s_waitcnt lgkmcnt(0)
	s_nop 1
	v_mov_b32_dpp v71, v90 quad_perm:[1,0,3,2] row_mask:0xf bank_mask:0xf
	s_mov_b64 s[2:3], exec
	s_and_b64 exec, s[2:3], s[82:83]
	v_mov_b32_e32 v70, v90
	s_waitcnt lgkmcnt(0)
	v_pk_mul_f32 v[70:71], v[70:71], v[188:189]
	s_nop 0
	v_add_f32_e32 v90, v70, v71
	s_and_b64 exec, s[2:3], s[84:85]
	v_mov_b32_e32 v72, v90
	v_mov_b32_e32 v73, v189
	s_waitcnt lgkmcnt(0)
	v_mov_b32_e32 v189, v71
	v_pk_mul_f32 v[70:71], v[72:73], v[188:189]
	s_nop 0
	v_sub_f32_e32 v90, v70, v71
	s_mov_b64 exec, s[2:3]
	s_waitcnt lgkmcnt(0)
	s_nop 1
	v_mov_b32_dpp v71, v91 quad_perm:[1,0,3,2] row_mask:0xf bank_mask:0xf
	s_mov_b64 s[2:3], exec
	s_and_b64 exec, s[2:3], s[82:83]
	v_mov_b32_e32 v70, v91
	s_waitcnt lgkmcnt(0)
	v_mul_f32_e32 v72, v71, v187
	v_pk_fma_f32 v[70:71], v[70:71], v[186:187], v[72:73] op_sel_hi:[1,1,0]
	s_nop 0
	v_mov_b32_e32 v91, v70
	s_and_b64 exec, s[2:3], s[84:85]
	v_mov_b32_e32 v72, v91
	v_mov_b32_e32 v73, v187
	v_mov_b32_e32 v70, v186
	s_waitcnt lgkmcnt(0)
	v_mul_f32_e32 v74, v187, v71
	v_pk_fma_f32 v[70:71], v[72:73], v[70:71], v[74:75] op_sel_hi:[1,1,0] neg_lo:[0,0,1] neg_hi:[0,0,1]
	s_nop 0
	v_mov_b32_e32 v91, v70
	s_mov_b64 exec, s[2:3]
	s_waitcnt lgkmcnt(0)
	s_nop 1
	v_mov_b32_dpp v71, v84 quad_perm:[1,0,3,2] row_mask:0xf bank_mask:0xf
	s_mov_b64 s[2:3], exec
	s_and_b64 exec, s[2:3], s[82:83]
	v_mov_b32_e32 v70, v84
	s_waitcnt lgkmcnt(0)
	v_pk_mul_f32 v[70:71], v[70:71], v[184:185]
	s_nop 0
	v_add_f32_e32 v84, v70, v71
	s_and_b64 exec, s[2:3], s[84:85]
	v_mov_b32_e32 v72, v84
	v_mov_b32_e32 v73, v185
	s_waitcnt lgkmcnt(0)
	v_mov_b32_e32 v185, v71
	v_pk_mul_f32 v[70:71], v[72:73], v[184:185]
	s_nop 0
	v_sub_f32_e32 v84, v70, v71
	s_mov_b64 exec, s[2:3]
	s_waitcnt lgkmcnt(0)
	s_nop 1
	v_mov_b32_dpp v71, v85 quad_perm:[1,0,3,2] row_mask:0xf bank_mask:0xf
	s_mov_b64 s[2:3], exec
	s_and_b64 exec, s[2:3], s[82:83]
	v_mov_b32_e32 v70, v85
	s_waitcnt lgkmcnt(0)
	v_mul_f32_e32 v72, v71, v183
	v_pk_fma_f32 v[70:71], v[70:71], v[182:183], v[72:73] op_sel_hi:[1,1,0]
	s_nop 0
	v_mov_b32_e32 v85, v70
	s_and_b64 exec, s[2:3], s[84:85]
	v_mov_b32_e32 v72, v85
	v_mov_b32_e32 v73, v183
	v_mov_b32_e32 v70, v182
	s_waitcnt lgkmcnt(0)
	v_mul_f32_e32 v74, v183, v71
	v_pk_fma_f32 v[70:71], v[72:73], v[70:71], v[74:75] op_sel_hi:[1,1,0] neg_lo:[0,0,1] neg_hi:[0,0,1]
	s_nop 0
	v_mov_b32_e32 v85, v70
	s_mov_b64 exec, s[2:3]
	s_waitcnt lgkmcnt(0)
	s_nop 1
	v_mov_b32_dpp v71, v78 quad_perm:[1,0,3,2] row_mask:0xf bank_mask:0xf
	s_mov_b64 s[2:3], exec
	s_and_b64 exec, s[2:3], s[82:83]
	v_mov_b32_e32 v70, v78
	s_waitcnt lgkmcnt(0)
	v_pk_mul_f32 v[70:71], v[70:71], v[180:181]
	s_nop 0
	v_add_f32_e32 v78, v70, v71
	s_and_b64 exec, s[2:3], s[84:85]
	v_mov_b32_e32 v72, v78
	v_mov_b32_e32 v73, v181
	s_waitcnt lgkmcnt(0)
	v_mov_b32_e32 v181, v71
	v_pk_mul_f32 v[70:71], v[72:73], v[180:181]
	s_nop 0
	v_sub_f32_e32 v78, v70, v71
	s_mov_b64 exec, s[2:3]
	s_waitcnt lgkmcnt(0)
	s_nop 1
	v_mov_b32_dpp v71, v79 quad_perm:[1,0,3,2] row_mask:0xf bank_mask:0xf
	s_mov_b64 s[2:3], exec
	s_and_b64 exec, s[2:3], s[82:83]
	v_mov_b32_e32 v70, v79
	s_waitcnt lgkmcnt(0)
	v_mul_f32_e32 v72, v71, v179
	v_pk_fma_f32 v[70:71], v[70:71], v[178:179], v[72:73] op_sel_hi:[1,1,0]
	s_nop 0
	v_mov_b32_e32 v79, v70
	s_and_b64 exec, s[2:3], s[84:85]
	v_mov_b32_e32 v72, v79
	v_mov_b32_e32 v73, v179
	v_mov_b32_e32 v70, v178
	s_waitcnt lgkmcnt(0)
	v_mul_f32_e32 v74, v179, v71
	v_pk_fma_f32 v[70:71], v[72:73], v[70:71], v[74:75] op_sel_hi:[1,1,0] neg_lo:[0,0,1] neg_hi:[0,0,1]
	s_nop 0
	v_mov_b32_e32 v79, v70
	s_mov_b64 exec, s[2:3]
	s_waitcnt lgkmcnt(0)
	s_nop 1
	v_mov_b32_dpp v71, v68 quad_perm:[1,0,3,2] row_mask:0xf bank_mask:0xf
	s_mov_b64 s[2:3], exec
	s_and_b64 exec, s[2:3], s[82:83]
	v_mov_b32_e32 v70, v68
	s_waitcnt lgkmcnt(0)
	v_pk_mul_f32 v[70:71], v[70:71], v[176:177]
	s_nop 0
	v_add_f32_e32 v68, v70, v71
	s_and_b64 exec, s[2:3], s[84:85]
	v_mov_b32_e32 v72, v68
	v_mov_b32_e32 v73, v177
	s_waitcnt lgkmcnt(0)
	v_mov_b32_e32 v177, v71
	v_pk_mul_f32 v[70:71], v[72:73], v[176:177]
	s_nop 0
	v_sub_f32_e32 v68, v70, v71
	s_mov_b64 exec, s[2:3]
	s_waitcnt lgkmcnt(0)
	s_nop 1
	v_mov_b32_dpp v71, v69 quad_perm:[1,0,3,2] row_mask:0xf bank_mask:0xf
	s_mov_b64 s[2:3], exec
	s_and_b64 exec, s[2:3], s[82:83]
	v_mov_b32_e32 v70, v69
	s_waitcnt lgkmcnt(0)
	v_mul_f32_e32 v72, v71, v175
	v_pk_fma_f32 v[70:71], v[70:71], v[174:175], v[72:73] op_sel_hi:[1,1,0]
	s_nop 0
	v_mov_b32_e32 v69, v70
	s_and_b64 exec, s[2:3], s[84:85]
	v_mov_b32_e32 v72, v69
	v_mov_b32_e32 v73, v175
	v_mov_b32_e32 v70, v174
	s_waitcnt lgkmcnt(0)
	v_mul_f32_e32 v74, v175, v71
	v_pk_fma_f32 v[70:71], v[72:73], v[70:71], v[74:75] op_sel_hi:[1,1,0] neg_lo:[0,0,1] neg_hi:[0,0,1]
	s_nop 0
	v_mov_b32_e32 v69, v70
	s_mov_b64 exec, s[2:3]
	s_waitcnt lgkmcnt(0)
	s_nop 1
	v_mov_b32_dpp v71, v66 quad_perm:[1,0,3,2] row_mask:0xf bank_mask:0xf
	s_mov_b64 s[2:3], exec
	s_and_b64 exec, s[2:3], s[82:83]
	v_mov_b32_e32 v70, v66
	s_waitcnt lgkmcnt(0)
	v_pk_mul_f32 v[70:71], v[70:71], v[172:173]
	s_nop 0
	v_add_f32_e32 v66, v70, v71
	s_and_b64 exec, s[2:3], s[84:85]
	v_mov_b32_e32 v72, v66
	v_mov_b32_e32 v73, v173
	s_waitcnt lgkmcnt(0)
	v_mov_b32_e32 v173, v71
	v_pk_mul_f32 v[70:71], v[72:73], v[172:173]
	s_nop 0
	v_sub_f32_e32 v66, v70, v71
	s_mov_b64 exec, s[2:3]
	s_waitcnt lgkmcnt(0)
	s_nop 1
	v_mov_b32_dpp v71, v67 quad_perm:[1,0,3,2] row_mask:0xf bank_mask:0xf
	s_mov_b64 s[2:3], exec
	s_and_b64 exec, s[2:3], s[82:83]
	v_mov_b32_e32 v70, v67
	s_waitcnt lgkmcnt(0)
	v_mul_f32_e32 v72, v71, v171
	v_pk_fma_f32 v[70:71], v[70:71], v[170:171], v[72:73] op_sel_hi:[1,1,0]
	s_nop 0
	v_mov_b32_e32 v67, v70
	s_and_b64 exec, s[2:3], s[84:85]
	v_mov_b32_e32 v72, v67
	v_mov_b32_e32 v73, v171
	v_mov_b32_e32 v70, v170
	s_waitcnt lgkmcnt(0)
	v_mul_f32_e32 v74, v171, v71
	v_pk_fma_f32 v[70:71], v[72:73], v[70:71], v[74:75] op_sel_hi:[1,1,0] neg_lo:[0,0,1] neg_hi:[0,0,1]
	s_nop 0
	v_mov_b32_e32 v67, v70
	s_mov_b64 exec, s[2:3]
	s_waitcnt lgkmcnt(0)
	s_nop 1
	v_mov_b32_dpp v71, v64 quad_perm:[1,0,3,2] row_mask:0xf bank_mask:0xf
	s_mov_b64 s[2:3], exec
	s_and_b64 exec, s[2:3], s[82:83]
	v_mov_b32_e32 v70, v64
	s_waitcnt lgkmcnt(0)
	v_pk_mul_f32 v[70:71], v[70:71], v[168:169]
	s_nop 0
	v_add_f32_e32 v64, v70, v71
	s_and_b64 exec, s[2:3], s[84:85]
	v_mov_b32_e32 v72, v64
	v_mov_b32_e32 v73, v169
	s_waitcnt lgkmcnt(0)
	v_mov_b32_e32 v169, v71
	v_pk_mul_f32 v[70:71], v[72:73], v[168:169]
	s_nop 0
	v_sub_f32_e32 v64, v70, v71
	s_mov_b64 exec, s[2:3]
	s_waitcnt lgkmcnt(0)
	s_nop 1
	v_mov_b32_dpp v71, v65 quad_perm:[1,0,3,2] row_mask:0xf bank_mask:0xf
	s_mov_b64 s[2:3], exec
	s_and_b64 exec, s[2:3], s[82:83]
	v_mov_b32_e32 v70, v65
	s_waitcnt lgkmcnt(0)
	v_mul_f32_e32 v72, v71, v167
	v_pk_fma_f32 v[70:71], v[70:71], v[166:167], v[72:73] op_sel_hi:[1,1,0]
	s_nop 0
	v_mov_b32_e32 v65, v70
	s_and_b64 exec, s[2:3], s[84:85]
	v_mov_b32_e32 v72, v65
	v_mov_b32_e32 v73, v167
	v_mov_b32_e32 v70, v166
	s_waitcnt lgkmcnt(0)
	v_mul_f32_e32 v74, v167, v71
	v_pk_fma_f32 v[70:71], v[72:73], v[70:71], v[74:75] op_sel_hi:[1,1,0] neg_lo:[0,0,1] neg_hi:[0,0,1]
	s_nop 0
	v_mov_b32_e32 v65, v70
	s_mov_b64 exec, s[2:3]
	s_waitcnt lgkmcnt(0)
	s_nop 1
	v_mov_b32_dpp v71, v62 quad_perm:[1,0,3,2] row_mask:0xf bank_mask:0xf
	s_mov_b64 s[2:3], exec
	s_and_b64 exec, s[2:3], s[82:83]
	v_mov_b32_e32 v70, v62
	s_waitcnt lgkmcnt(0)
	v_pk_mul_f32 v[70:71], v[70:71], v[88:89]
	s_nop 0
	v_add_f32_e32 v62, v70, v71
	s_and_b64 exec, s[2:3], s[84:85]
	v_mov_b32_e32 v72, v62
	v_mov_b32_e32 v73, v89
	s_waitcnt lgkmcnt(0)
	v_mov_b32_e32 v89, v71
	v_pk_mul_f32 v[70:71], v[72:73], v[88:89]
	s_nop 0
	v_sub_f32_e32 v62, v70, v71
	s_mov_b64 exec, s[2:3]
	s_waitcnt lgkmcnt(0)
	s_nop 1
	v_mov_b32_dpp v71, v63 quad_perm:[1,0,3,2] row_mask:0xf bank_mask:0xf
	v_cmp_lt_i32_e32 vcc, 0, v96
	s_and_saveexec_b64 s[2:3], vcc
	s_xor_b64 s[2:3], exec, s[2:3]
	s_cbranch_execz .LBB0_755
	v_cmp_eq_u32_e32 vcc, 1, v96
	s_and_saveexec_b64 s[10:11], vcc
	s_cbranch_execz .LBB0_752
	v_mov_b32_e32 v70, v63
	s_waitcnt lgkmcnt(0)
	v_mul_f32_e32 v72, v71, v87
	v_pk_fma_f32 v[70:71], v[70:71], v[86:87], v[72:73] op_sel_hi:[1,1,0]
	s_nop 0
	v_mov_b32_e32 v63, v70

.LBB0_759:
	s_or_b64 exec, exec, s[2:3]
	v_lshlrev_b32_e32 v74, 16, v50
	ds_bpermute_b32 v76, v232, v98
	ds_bpermute_b32 v75, v232, v163
	ds_bpermute_b32 v72, v233, v98
	ds_bpermute_b32 v73, v233, v163
	ds_bpermute_b32 v70, v234, v98
	ds_bpermute_b32 v63, v234, v163
	ds_bpermute_b32 v68, v235, v98
	ds_bpermute_b32 v69, v235, v163
	ds_bpermute_b32 v66, v236, v98
	ds_bpermute_b32 v65, v236, v163
	ds_bpermute_b32 v60, v237, v98
	ds_bpermute_b32 v61, v237, v163
	ds_bpermute_b32 v58, v238, v98
	ds_bpermute_b32 v57, v238, v163
	ds_bpermute_b32 v54, v239, v98
	ds_bpermute_b32 v55, v239, v163
	s_nop 1
	v_mov_b32_dpp v77, v74 quad_perm:[1,0,3,2] row_mask:0xf bank_mask:0xf
	v_and_b32_e32 v1, 0xffff0000, v50
	s_mov_b64 s[2:3], exec
	s_and_b64 exec, s[2:3], s[82:83]
	s_waitcnt lgkmcnt(0)
	v_pk_mul_f32 v[74:75], v[74:75], v[76:77]
	s_nop 0
	v_add_f32_e32 v74, v74, v75
	s_and_b64 exec, s[2:3], s[84:85]
	s_waitcnt lgkmcnt(0)
	v_pk_mul_f32 v[74:75], v[74:75], v[76:77]
	s_nop 0
	v_sub_f32_e32 v74, v74, v75
	s_mov_b64 exec, s[2:3]
	s_waitcnt lgkmcnt(13)
	s_nop 1
	v_mov_b32_dpp v75, v1 quad_perm:[1,0,3,2] row_mask:0xf bank_mask:0xf
	v_mov_b32_e32 v50, v74
	s_mov_b64 s[2:3], exec
	s_and_b64 exec, s[2:3], s[82:83]
	v_mov_b32_e32 v76, v1
	s_waitcnt lgkmcnt(0)
	v_mov_b32_e32 v77, v73
	s_waitcnt lgkmcnt(0)
	v_mov_b32_e32 v73, v75
	v_mul_f32_e32 v56, v1, v72
	v_pk_fma_f32 v[72:73], v[76:77], v[72:73], v[56:57] op_sel_hi:[1,1,0]
	s_nop 0
	v_mov_b32_e32 v1, v73
	s_and_b64 exec, s[2:3], s[84:85]
	v_mov_b32_e32 v74, v1
	v_mul_f32_e32 v56, v1, v72
	s_waitcnt lgkmcnt(0)
	v_pk_fma_f32 v[72:73], v[74:75], v[72:73], v[56:57] op_sel_hi:[1,1,0] neg_lo:[1,0,0] neg_hi:[1,0,0]
	s_nop 0
	v_mov_b32_e32 v1, v73
	s_mov_b64 exec, s[2:3]
	v_lshlrev_b32_e32 v62, 16, v51
	s_nop 1
	v_mov_b32_dpp v71, v62 quad_perm:[1,0,3,2] row_mask:0xf bank_mask:0xf
	v_and_b32_e32 v51, 0xffff0000, v51
	s_mov_b64 s[2:3], exec
	s_and_b64 exec, s[2:3], s[82:83]
	s_waitcnt lgkmcnt(0)
	v_pk_mul_f32 v[62:63], v[70:71], v[62:63]
	s_nop 0
	v_add_f32_e32 v62, v62, v63
	s_and_b64 exec, s[2:3], s[84:85]
	s_waitcnt lgkmcnt(0)
	v_pk_mul_f32 v[62:63], v[70:71], v[62:63]
	s_nop 0
	v_sub_f32_e32 v62, v62, v63
	s_mov_b64 exec, s[2:3]
	s_waitcnt lgkmcnt(0)
	s_nop 1
	v_mov_b32_dpp v71, v51 quad_perm:[1,0,3,2] row_mask:0xf bank_mask:0xf
	s_mov_b64 s[2:3], exec
	s_and_b64 exec, s[2:3], s[82:83]
	v_mov_b32_e32 v72, v51
	v_mov_b32_e32 v73, v69
	s_waitcnt lgkmcnt(0)
	v_mov_b32_e32 v69, v71
	v_mul_f32_e32 v56, v51, v68
	v_pk_fma_f32 v[68:69], v[72:73], v[68:69], v[56:57] op_sel_hi:[1,1,0]
	s_nop 0
	v_mov_b32_e32 v51, v69
	s_and_b64 exec, s[2:3], s[84:85]
	v_mov_b32_e32 v70, v51
	v_mul_f32_e32 v56, v51, v68
	s_waitcnt lgkmcnt(0)
	v_pk_fma_f32 v[68:69], v[70:71], v[68:69], v[56:57] op_sel_hi:[1,1,0] neg_lo:[1,0,0] neg_hi:[1,0,0]
	s_nop 0
	v_mov_b32_e32 v51, v69
	s_mov_b64 exec, s[2:3]
	v_lshlrev_b32_e32 v64, 16, v52
	s_nop 1
	v_mov_b32_dpp v67, v64 quad_perm:[1,0,3,2] row_mask:0xf bank_mask:0xf
	v_and_b32_e32 v63, 0xffff0000, v52
	s_mov_b64 s[2:3], exec
	s_and_b64 exec, s[2:3], s[82:83]
	s_waitcnt lgkmcnt(0)
	v_pk_mul_f32 v[64:65], v[66:67], v[64:65]
	s_nop 0
	v_add_f32_e32 v64, v64, v65
	s_and_b64 exec, s[2:3], s[84:85]
	s_waitcnt lgkmcnt(0)
	v_pk_mul_f32 v[64:65], v[66:67], v[64:65]
	s_nop 0
	v_sub_f32_e32 v64, v64, v65
	s_mov_b64 exec, s[2:3]
	s_waitcnt lgkmcnt(0)
	s_nop 1
	v_mov_b32_dpp v67, v63 quad_perm:[1,0,3,2] row_mask:0xf bank_mask:0xf
	s_mov_b64 s[2:3], exec
	s_and_b64 exec, s[2:3], s[82:83]
	v_mov_b32_e32 v68, v63
	v_mov_b32_e32 v69, v61
	s_waitcnt lgkmcnt(0)
	v_mov_b32_e32 v61, v67
	v_mul_f32_e32 v52, v63, v60
	v_pk_fma_f32 v[60:61], v[68:69], v[60:61], v[52:53] op_sel_hi:[1,1,0]
	s_nop 0
	v_mov_b32_e32 v63, v61
	s_and_b64 exec, s[2:3], s[84:85]
	v_mov_b32_e32 v66, v63
	v_mul_f32_e32 v52, v63, v60
	s_waitcnt lgkmcnt(0)
	v_pk_fma_f32 v[60:61], v[66:67], v[60:61], v[52:53] op_sel_hi:[1,1,0] neg_lo:[1,0,0] neg_hi:[1,0,0]
	s_nop 0
	v_mov_b32_e32 v63, v61
	s_mov_b64 exec, s[2:3]
	v_lshlrev_b32_e32 v56, 16, v53
	s_nop 1
	v_mov_b32_dpp v59, v56 quad_perm:[1,0,3,2] row_mask:0xf bank_mask:0xf
	v_and_b32_e32 v53, 0xffff0000, v53
	s_mov_b64 s[2:3], exec
	s_and_b64 exec, s[2:3], s[82:83]
	s_waitcnt lgkmcnt(0)
	v_pk_mul_f32 v[56:57], v[58:59], v[56:57]
	s_nop 0
	v_add_f32_e32 v56, v56, v57
	s_and_b64 exec, s[2:3], s[84:85]
	s_waitcnt lgkmcnt(0)
	v_pk_mul_f32 v[56:57], v[58:59], v[56:57]
	s_nop 0
	v_sub_f32_e32 v56, v56, v57
	s_mov_b64 exec, s[2:3]
	s_waitcnt lgkmcnt(0)
	s_nop 1
	v_mov_b32_dpp v59, v53 quad_perm:[1,0,3,2] row_mask:0xf bank_mask:0xf
	s_mov_b64 s[2:3], exec
	s_and_b64 exec, s[2:3], s[82:83]
	v_mov_b32_e32 v60, v53
	v_mov_b32_e32 v61, v55
	s_waitcnt lgkmcnt(0)
	v_mov_b32_e32 v55, v59
	v_mul_f32_e32 v52, v53, v54
	v_pk_fma_f32 v[52:53], v[60:61], v[54:55], v[52:53] op_sel_hi:[1,1,0]
	s_and_b64 exec, s[2:3], s[84:85]
	v_mov_b32_e32 v58, v53
	v_mul_f32_e32 v52, v53, v54
	s_waitcnt lgkmcnt(0)
	v_pk_fma_f32 v[52:53], v[58:59], v[54:55], v[52:53] op_sel_hi:[1,1,0] neg_lo:[1,0,0] neg_hi:[1,0,0]
	s_mov_b64 exec, s[2:3]
	v_lshl_add_u64 v[54:55], s[88:89], 0, v[154:155]
	v_cvt_pk_bf16_f32 v50, v50, v1
	v_cvt_pk_bf16_f32 v51, v62, v51
	v_cvt_pk_bf16_f32 v52, v64, v63
	v_cvt_pk_bf16_f32 v53, v56, v53
	global_store_dwordx4 v[54:55], v[50:53], off
	global_load_dword v1, v[106:107], off
	v_and_or_b32 v56, v94, 15, v215
	v_mul_f32_e32 v50, v249, v249
	ds_bpermute_b32 v50, v211, v50
	v_ashrrev_i32_e32 v52, 4, v94
	s_waitcnt lgkmcnt(0)
	v_fmac_f32_e32 v50, v249, v249
	ds_bpermute_b32 v51, v212, v50
	s_waitcnt lgkmcnt(0)
	v_add_f32_e32 v50, v50, v51
	ds_bpermute_b32 v51, v213, v50
	s_waitcnt lgkmcnt(0)
	v_add_f32_e32 v50, v50, v51
	ds_bpermute_b32 v51, v210, v50
	s_waitcnt lgkmcnt(0)
	v_add_f32_e32 v50, v50, v51
	ds_bpermute_b32 v51, v209, v50
	s_waitcnt lgkmcnt(0)
	v_add_f32_e32 v53, v50, v51
	s_nop 1
	v_mov_b32_dpp v54, v53 quad_perm:[1,0,3,2] row_mask:0xf bank_mask:0xf
	ds_bpermute_b32 v50, v214, v98
	ds_bpermute_b32 v51, v214, v163
	v_lshlrev_b32_e32 v98, 4, v56
	v_mov_b32_e32 v163, v99
	s_waitcnt lgkmcnt(2)
	v_add_f32_e32 v53, v53, v54
	v_fmamk_f32 v53, v53, 0x3c800000, v95
	v_mul_f32_e32 v54, 0x4b800000, v53
	v_cmp_gt_f32_e32 vcc, s50, v53
	s_nop 1
	v_cndmask_b32_e32 v53, v53, v54, vcc
	v_rsq_f32_e32 v54, v53
	v_ashrrev_i32_e32 v53, 31, v52
	v_lshlrev_b64 v[52:53], 11, v[52:53]
	v_lshl_add_u64 v[52:53], v[100:101], 0, v[52:53]
	v_mul_f32_e32 v55, 0x45800000, v54
	v_cndmask_b32_e32 v54, v54, v55, vcc
	v_mul_f32_e32 v54, v249, v54
	v_lshl_add_u64 v[52:53], v[52:53], 0, v[98:99]
	s_waitcnt vmcnt(0)
	v_mul_f32_e32 v54, v1, v54
	ds_bpermute_b32 v55, v213, v54
	s_waitcnt lgkmcnt(0)
	v_pk_mul_f32 v[50:51], v[54:55], v[50:51]
	s_nop 0
	v_sub_f32_e32 v1, v50, v51
	v_add_f32_e32 v50, v51, v50
	v_cndmask_b32_e64 v50, v54, v50, s[0:1]
	v_cndmask_b32_e64 v1, v50, v1, s[6:7]
	v_cvt_pk_bf16_f32 v1, v1, s0
	v_lshl_add_u64 v[50:51], v[52:53], 0, v[162:163]
	global_store_short v[50:51], v1, off
	s_and_saveexec_b64 s[2:3], s[6:7]
	s_cbranch_execz .LBB0_809
	v_mul_f32_e32 v1, 0x3d3504f3, v248
	v_lshl_add_u64 v[50:51], s[88:89], 0, v[140:141]
	global_store_dword v[50:51], v1, off
